# v48: v46 + batched LDS reads: attention pass-prologue QK^T(0) K fragments (both loops) and the MoE rank-assignment loop (8 entries per wait)
# speedup vs baseline: 1.0154x; 1.0038x over previous
.LBB0_1032:
	v_lshlrev_b32_e32 v3, 10, v118
	v_lshlrev_b32_e32 v4, 4, v117
	v_add3_u32 v107, 0, v3, v4
	ds_read_b128 v[144:147], v107
	ds_read_b128 v[148:151], v107 offset:512
	ds_read_b128 v[152:155], v107 offset:2048
	ds_read_b128 v[156:159], v107 offset:2560
	ds_read_b128 v[160:163], v107 offset:4096
	ds_read_b128 v[164:167], v107 offset:4608
	ds_read_b128 v[168:171], v107 offset:6144
	ds_read_b128 v[172:175], v107 offset:6656
	ds_read_b128 v[176:179], v107 offset:8192
	ds_read_b128 v[180:183], v107 offset:8704
	ds_read_b128 v[188:191], v107 offset:10240
	ds_read_b128 v[192:195], v107 offset:10752
	s_mov_b64 s[4:5], -1
	s_and_b64 vcc, exec, s[6:7]
	s_waitcnt vmcnt(5) lgkmcnt(11)
	v_mfma_f32_32x32x16_bf16 v[50:65], v[144:147], v[66:69], 0
	s_waitcnt lgkmcnt(10)
	v_mfma_f32_32x32x16_bf16 v[34:49], v[148:151], v[66:69], 0
	s_waitcnt vmcnt(4) lgkmcnt(9)
	v_mfma_f32_32x32x16_bf16 v[50:65], v[152:155], v[70:73], v[50:65]
	s_waitcnt lgkmcnt(8)
	v_mfma_f32_32x32x16_bf16 v[34:49], v[156:159], v[70:73], v[34:49]
	s_waitcnt vmcnt(3) lgkmcnt(7)
	v_mfma_f32_32x32x16_bf16 v[50:65], v[160:163], v[74:77], v[50:65]
	s_waitcnt lgkmcnt(6)
	v_mfma_f32_32x32x16_bf16 v[34:49], v[164:167], v[74:77], v[34:49]
	s_waitcnt vmcnt(2) lgkmcnt(5)
	v_mfma_f32_32x32x16_bf16 v[50:65], v[168:171], v[78:81], v[50:65]
	s_waitcnt lgkmcnt(4)
	v_mfma_f32_32x32x16_bf16 v[34:49], v[172:175], v[78:81], v[34:49]
	s_waitcnt vmcnt(1) lgkmcnt(3)
	v_mfma_f32_32x32x16_bf16 v[50:65], v[176:179], v[82:85], v[50:65]
	s_waitcnt lgkmcnt(2)
	v_mfma_f32_32x32x16_bf16 v[34:49], v[180:183], v[82:85], v[34:49]
	s_waitcnt vmcnt(0) lgkmcnt(1)
	v_mfma_f32_32x32x16_bf16 v[50:65], v[188:191], v[86:89], v[50:65]
	s_waitcnt lgkmcnt(0)
	v_mfma_f32_32x32x16_bf16 v[34:49], v[192:195], v[86:89], v[34:49]
	s_cbranch_vccnz .LBB0_1034
	s_waitcnt vmcnt(2) lgkmcnt(0)
	s_barrier
	s_mov_b64 s[4:5], 0

.LBB0_1083:
	ds_read_b128 v[2:5], v191
	ds_read_b128 v[6:9], v191 offset:512
	ds_read_b128 v[10:13], v191 offset:2048
	ds_read_b128 v[14:17], v191 offset:2560
	ds_read_b128 v[18:21], v191 offset:4096
	ds_read_b128 v[22:25], v191 offset:4608
	ds_read_b128 v[26:29], v191 offset:6144
	ds_read_b128 v[30:33], v191 offset:6656
	global_load_dword v0, v1, s[96:97]
	s_mov_b64 s[2:3], -1
	s_and_b64 vcc, exec, s[6:7]
	s_waitcnt vmcnt(4) lgkmcnt(7)
	v_mfma_f32_32x32x16_bf16 v[66:81], v[2:5], v[98:101], 0
	s_waitcnt lgkmcnt(6)
	v_mfma_f32_32x32x16_bf16 v[82:97], v[6:9], v[98:101], 0
	s_waitcnt vmcnt(3) lgkmcnt(5)
	v_mfma_f32_32x32x16_bf16 v[66:81], v[10:13], v[102:105], v[66:81]
	s_waitcnt lgkmcnt(4)
	v_mfma_f32_32x32x16_bf16 v[82:97], v[14:17], v[102:105], v[82:97]
	s_waitcnt vmcnt(2) lgkmcnt(3)
	v_mfma_f32_32x32x16_bf16 v[66:81], v[18:21], v[106:109], v[66:81]
	s_waitcnt lgkmcnt(2)
	v_mfma_f32_32x32x16_bf16 v[82:97], v[22:25], v[106:109], v[82:97]
	s_waitcnt vmcnt(1) lgkmcnt(1)
	v_mfma_f32_32x32x16_bf16 v[66:81], v[26:29], v[110:113], v[66:81]
	s_waitcnt lgkmcnt(0)
	v_mfma_f32_32x32x16_bf16 v[82:97], v[30:33], v[110:113], v[82:97]
	s_cbranch_vccnz .LBB0_1085
	s_waitcnt vmcnt(3) lgkmcnt(0)
	s_barrier
	s_mov_b64 s[2:3], 0

.LBB0_1313:
	s_add_i32 s5, s4, 0
	v_mov_b32_e32 v3, s5
	ds_read_b32 v5, v3 offset:40960
	ds_read_b32 v6, v3 offset:40964
	ds_read_b32 v7, v3 offset:40968
	ds_read_b32 v8, v3 offset:40972
	ds_read_b32 v9, v3 offset:40976
	ds_read_b32 v10, v3 offset:40980
	ds_read_b32 v11, v3 offset:40984
	ds_read_b32 v12, v3 offset:40988
	s_waitcnt lgkmcnt(7)
	v_cmp_eq_u32_e32 vcc, v5, v50
	s_and_saveexec_b64 s[2:3], vcc
	ds_write_b32 v3, v0 offset:41984
	v_add_u32_e32 v0, 1, v0
	s_or_b64 exec, exec, s[2:3]
	s_waitcnt lgkmcnt(7)
	v_cmp_eq_u32_e32 vcc, v6, v50
	s_and_saveexec_b64 s[2:3], vcc
	ds_write_b32 v3, v0 offset:41988
	v_add_u32_e32 v0, 1, v0
	s_or_b64 exec, exec, s[2:3]
	s_waitcnt lgkmcnt(7)
	v_cmp_eq_u32_e32 vcc, v7, v50
	s_and_saveexec_b64 s[2:3], vcc
	ds_write_b32 v3, v0 offset:41992
	v_add_u32_e32 v0, 1, v0
	s_or_b64 exec, exec, s[2:3]
	s_waitcnt lgkmcnt(7)
	v_cmp_eq_u32_e32 vcc, v8, v50
	s_and_saveexec_b64 s[2:3], vcc
	ds_write_b32 v3, v0 offset:41996
	v_add_u32_e32 v0, 1, v0
	s_or_b64 exec, exec, s[2:3]
	s_waitcnt lgkmcnt(7)
	v_cmp_eq_u32_e32 vcc, v9, v50
	s_and_saveexec_b64 s[2:3], vcc
	ds_write_b32 v3, v0 offset:42000
	v_add_u32_e32 v0, 1, v0
	s_or_b64 exec, exec, s[2:3]
	s_waitcnt lgkmcnt(7)
	v_cmp_eq_u32_e32 vcc, v10, v50
	s_and_saveexec_b64 s[2:3], vcc
	ds_write_b32 v3, v0 offset:42004
	v_add_u32_e32 v0, 1, v0
	s_or_b64 exec, exec, s[2:3]
	s_waitcnt lgkmcnt(7)
	v_cmp_eq_u32_e32 vcc, v11, v50
	s_and_saveexec_b64 s[2:3], vcc
	ds_write_b32 v3, v0 offset:42008
	v_add_u32_e32 v0, 1, v0
	s_or_b64 exec, exec, s[2:3]
	s_waitcnt lgkmcnt(7)
	v_cmp_eq_u32_e32 vcc, v12, v50
	s_and_saveexec_b64 s[2:3], vcc
	ds_write_b32 v3, v0 offset:42012
	v_add_u32_e32 v0, 1, v0
	s_branch .LBB0_1312
